# v31: v21 + MoE scatter phase: count-table copies global->LDS issued 16 loads per batch (3 round trips instead of 20)
# speedup vs baseline: 1.0067x; 1.0067x over previous
.LBB0_1379:
	s_andn2_b64 vcc, exec, s[2:3]
	s_cbranch_vccnz .LBB0_1700
	v_mov_b32_e32 v20, v0
	s_nop 0
	v_readfirstlane_b32 s10, v20
	v_readlane_b32 s12, v252, 15
	v_readlane_b32 s13, v252, 16
	s_mov_b64 s[2:3], exec
	v_lshlrev_b32_e32 v1, 2, v20
	v_add_u32_e32 v2, 0x10000, v1
	s_nop 3
	global_load_dword v54, v1, s[12:13]
	global_load_dword v55, v1, s[12:13] offset:2048
	s_add_u32 s4, s12, 0x1000
	s_addc_u32 s5, s13, 0
	global_load_dword v56, v1, s[4:5]
	global_load_dword v57, v1, s[4:5] offset:2048
	s_add_u32 s6, s12, 0x2000
	s_addc_u32 s7, s13, 0
	global_load_dword v58, v1, s[6:7]
	global_load_dword v59, v1, s[6:7] offset:2048
	s_add_u32 s8, s12, 0x3000
	s_addc_u32 s9, s13, 0
	global_load_dword v60, v1, s[8:9]
	global_load_dword v61, v1, s[8:9] offset:2048
	global_load_dword v62, v1, s[34:35]
	global_load_dword v63, v1, s[34:35] offset:2048
	s_add_u32 s4, s34, 0x1000
	s_addc_u32 s5, s35, 0
	global_load_dword v64, v1, s[4:5]
	global_load_dword v65, v1, s[4:5] offset:2048
	s_add_u32 s6, s34, 0x2000
	s_addc_u32 s7, s35, 0
	global_load_dword v66, v1, s[6:7]
	global_load_dword v67, v1, s[6:7] offset:2048
	s_add_u32 s8, s34, 0x3000
	s_addc_u32 s9, s35, 0
	global_load_dword v68, v1, s[8:9]
	global_load_dword v69, v1, s[8:9] offset:2048
	s_waitcnt vmcnt(0) lgkmcnt(0)
	ds_write_b32 v1, v54
	ds_write_b32 v1, v55 offset:2048
	ds_write_b32 v1, v56 offset:4096
	ds_write_b32 v1, v57 offset:6144
	ds_write_b32 v1, v58 offset:8192
	ds_write_b32 v1, v59 offset:10240
	ds_write_b32 v1, v60 offset:12288
	ds_write_b32 v1, v61 offset:14336
	ds_write_b32 v1, v62 offset:16384
	ds_write_b32 v1, v63 offset:18432
	ds_write_b32 v1, v64 offset:20480
	ds_write_b32 v1, v65 offset:22528
	ds_write_b32 v1, v66 offset:24576
	ds_write_b32 v1, v67 offset:26624
	ds_write_b32 v1, v68 offset:28672
	ds_write_b32 v1, v69 offset:30720
	s_add_u32 s0, s34, 0x4000
	s_addc_u32 s1, s35, 0
	global_load_dword v54, v1, s[0:1]
	global_load_dword v55, v1, s[0:1] offset:2048
	s_add_u32 s4, s34, 0x5000
	s_addc_u32 s5, s35, 0
	global_load_dword v56, v1, s[4:5]
	global_load_dword v57, v1, s[4:5] offset:2048
	s_add_u32 s6, s34, 0x6000
	s_addc_u32 s7, s35, 0
	global_load_dword v58, v1, s[6:7]
	global_load_dword v59, v1, s[6:7] offset:2048
	s_add_u32 s8, s34, 0x7000
	s_addc_u32 s9, s35, 0
	global_load_dword v60, v1, s[8:9]
	global_load_dword v61, v1, s[8:9] offset:2048
	s_add_u32 s0, s34, 0x8000
	s_addc_u32 s1, s35, 0
	global_load_dword v62, v1, s[0:1]
	global_load_dword v63, v1, s[0:1] offset:2048
	s_add_u32 s4, s34, 0x9000
	s_addc_u32 s5, s35, 0
	global_load_dword v64, v1, s[4:5]
	global_load_dword v65, v1, s[4:5] offset:2048
	s_add_u32 s6, s34, 0xa000
	s_addc_u32 s7, s35, 0
	global_load_dword v66, v1, s[6:7]
	global_load_dword v67, v1, s[6:7] offset:2048
	s_add_u32 s8, s34, 0xb000
	s_addc_u32 s9, s35, 0
	global_load_dword v68, v1, s[8:9]
	global_load_dword v69, v1, s[8:9] offset:2048
	s_waitcnt vmcnt(0)
	ds_write_b32 v1, v54 offset:32768
	ds_write_b32 v1, v55 offset:34816
	ds_write_b32 v1, v56 offset:36864
	ds_write_b32 v1, v57 offset:38912
	ds_write_b32 v1, v58 offset:40960
	ds_write_b32 v1, v59 offset:43008
	ds_write_b32 v1, v60 offset:45056
	ds_write_b32 v1, v61 offset:47104
	ds_write_b32 v1, v62 offset:49152
	ds_write_b32 v1, v63 offset:51200
	ds_write_b32 v1, v64 offset:53248
	ds_write_b32 v1, v65 offset:55296
	ds_write_b32 v1, v66 offset:57344
	ds_write_b32 v1, v67 offset:59392
	ds_write_b32 v1, v68 offset:61440
	ds_write_b32 v1, v69 offset:63488
	s_add_u32 s0, s34, 0xc000
	s_addc_u32 s1, s35, 0
	global_load_dword v54, v1, s[0:1]
	global_load_dword v55, v1, s[0:1] offset:2048
	s_add_u32 s4, s34, 0xd000
	s_addc_u32 s5, s35, 0
	global_load_dword v56, v1, s[4:5]
	global_load_dword v57, v1, s[4:5] offset:2048
	s_add_u32 s6, s34, 0xe000
	s_addc_u32 s7, s35, 0
	global_load_dword v58, v1, s[6:7]
	global_load_dword v59, v1, s[6:7] offset:2048
	s_add_u32 s8, s34, 0xf000
	s_addc_u32 s9, s35, 0
	global_load_dword v60, v1, s[8:9]
	global_load_dword v61, v1, s[8:9] offset:2048
	s_waitcnt vmcnt(0)
	ds_write_b32 v2, v54
	ds_write_b32 v2, v55 offset:2048
	ds_write_b32 v2, v56 offset:4096
	ds_write_b32 v2, v57 offset:6144
	ds_write_b32 v2, v58 offset:8192
	ds_write_b32 v2, v59 offset:10240
	ds_write_b32 v2, v60 offset:12288
	ds_write_b32 v2, v61 offset:14336
	v_add_u32_e32 v21, 0x200, v20
